# router phase stores sc1 too (TokInfo, lists): L2 clean at the grid barrier after the router
# baseline (speedup 1.0000x reference)
.LBB0_739:
	s_or_b64 exec, exec, s[0:1]
	s_waitcnt lgkmcnt(0)
	s_barrier
	s_and_saveexec_b64 s[0:1], s[14:15]
	s_cbranch_execz .LBB0_728
	v_lshl_add_u32 v7, v2, 2, 0
	v_lshl_add_u32 v8, v6, 2, 0
	ds_read_b32 v7, v7 offset:32896
	ds_read_b32 v9, v8 offset:32896
	v_readlane_b32 s4, v254, 54
	v_readlane_b32 s5, v254, 55
	v_add_u32_e32 v8, s19, v37
	s_waitcnt lgkmcnt(1)
	v_add_u32_e32 v10, v7, v4
	s_waitcnt lgkmcnt(0)
	v_add_u32_e32 v12, v9, v5
	v_lshlrev_b64 v[4:5], 17, v[2:3]
	v_ashrrev_i32_e32 v11, 31, v10
	v_lshl_add_u64 v[4:5], s[4:5], 0, v[4:5]
	v_lshl_add_u64 v[4:5], v[10:11], 2, v[4:5]
	v_ashrrev_i32_e32 v7, 31, v6
	global_store_dword v[4:5], v8, off sc1
	v_lshlrev_b64 v[4:5], 17, v[6:7]
	v_ashrrev_i32_e32 v13, 31, v12
	v_lshl_add_u64 v[4:5], s[4:5], 0, v[4:5]
	v_lshl_add_u64 v[4:5], v[12:13], 2, v[4:5]
	v_ashrrev_i32_e32 v9, 31, v8
	v_readlane_b32 s4, v254, 52
	global_store_dword v[4:5], v8, off sc1
	v_lshlrev_b64 v[4:5], 5, v[8:9]
	v_readlane_b32 s5, v254, 53
	v_mov_b32_e32 v7, v12
	s_nop 0
	v_lshl_add_u64 v[8:9], s[4:5], 0, v[4:5]
	v_mov_b32_e32 v4, v2
	v_mov_b32_e32 v5, v10
	v_mov_b32_e32 v2, v3
	global_store_dwordx4 v[8:9], v[4:7], off sc1
	global_store_dwordx4 v[8:9], v[0:3], off offset:16 sc1
	s_branch .LBB0_728

.LBB0_1616:
	s_or_b64 exec, exec, s[0:1]
	s_waitcnt lgkmcnt(0)
	s_barrier
	s_and_saveexec_b64 s[0:1], s[34:35]
	s_cbranch_execz .LBB0_1605
	v_lshl_add_u32 v7, v2, 2, 0
	v_lshl_add_u32 v53, v6, 2, 0
	ds_read_b32 v7, v7 offset:32896
	ds_read_b32 v53, v53 offset:32896
	v_readlane_b32 s4, v254, 54
	v_readlane_b32 s5, v254, 55
	v_add_u32_e32 v54, s19, v9
	s_waitcnt lgkmcnt(1)
	v_add_u32_e32 v56, v7, v4
	s_waitcnt lgkmcnt(0)
	v_add_u32_e32 v58, v53, v5
	v_lshlrev_b64 v[4:5], 17, v[2:3]
	v_ashrrev_i32_e32 v57, 31, v56
	v_lshl_add_u64 v[4:5], s[4:5], 0, v[4:5]
	v_lshl_add_u64 v[4:5], v[56:57], 2, v[4:5]
	v_ashrrev_i32_e32 v7, 31, v6
	global_store_dword v[4:5], v54, off sc1
	v_lshlrev_b64 v[4:5], 17, v[6:7]
	v_ashrrev_i32_e32 v59, 31, v58
	v_lshl_add_u64 v[4:5], s[4:5], 0, v[4:5]
	v_lshl_add_u64 v[4:5], v[58:59], 2, v[4:5]
	v_ashrrev_i32_e32 v55, 31, v54
	v_readlane_b32 s4, v254, 52
	global_store_dword v[4:5], v54, off sc1
	v_lshlrev_b64 v[4:5], 5, v[54:55]
	v_readlane_b32 s5, v254, 53
	v_mov_b32_e32 v7, v58
	s_nop 0
	v_lshl_add_u64 v[54:55], s[4:5], 0, v[4:5]
	v_mov_b32_e32 v4, v2
	v_mov_b32_e32 v5, v56
	v_mov_b32_e32 v2, v3
	global_store_dwordx4 v[54:55], v[4:7], off sc1
	global_store_dwordx4 v[54:55], v[0:3], off offset:16 sc1
	s_branch .LBB0_1605

.LBB0_2495:
	s_or_b64 exec, exec, s[0:1]
	s_waitcnt lgkmcnt(0)
	s_barrier
	s_and_saveexec_b64 s[0:1], s[26:27]
	s_cbranch_execz .LBB0_2484
	v_lshl_add_u32 v7, v2, 2, 0
	v_lshl_add_u32 v53, v6, 2, 0
	ds_read_b32 v7, v7 offset:32896
	ds_read_b32 v53, v53 offset:32896
	v_readlane_b32 s4, v254, 54
	v_readlane_b32 s5, v254, 55
	v_add_u32_e32 v54, s31, v9
	s_waitcnt lgkmcnt(1)
	v_add_u32_e32 v56, v7, v4
	s_waitcnt lgkmcnt(0)
	v_add_u32_e32 v58, v53, v5
	v_lshlrev_b64 v[4:5], 17, v[2:3]
	v_ashrrev_i32_e32 v57, 31, v56
	v_lshl_add_u64 v[4:5], s[4:5], 0, v[4:5]
	v_lshl_add_u64 v[4:5], v[56:57], 2, v[4:5]
	v_ashrrev_i32_e32 v7, 31, v6
	global_store_dword v[4:5], v54, off sc1
	v_lshlrev_b64 v[4:5], 17, v[6:7]
	v_ashrrev_i32_e32 v59, 31, v58
	v_lshl_add_u64 v[4:5], s[4:5], 0, v[4:5]
	v_lshl_add_u64 v[4:5], v[58:59], 2, v[4:5]
	v_ashrrev_i32_e32 v55, 31, v54
	v_readlane_b32 s4, v254, 52
	global_store_dword v[4:5], v54, off sc1
	v_lshlrev_b64 v[4:5], 5, v[54:55]
	v_readlane_b32 s5, v254, 53
	v_mov_b32_e32 v7, v58
	s_nop 0
	v_lshl_add_u64 v[54:55], s[4:5], 0, v[4:5]
	v_mov_b32_e32 v4, v2
	v_mov_b32_e32 v5, v56
	v_mov_b32_e32 v2, v3
	global_store_dwordx4 v[54:55], v[4:7], off sc1
	global_store_dwordx4 v[54:55], v[0:3], off offset:16 sc1
	s_branch .LBB0_2484

.LBB0_3243:
	s_or_b64 exec, exec, s[0:1]
	s_waitcnt lgkmcnt(0)
	s_barrier
	s_and_saveexec_b64 s[0:1], s[24:25]
	s_cbranch_execz .LBB0_3232
	v_lshl_add_u32 v7, v2, 2, 0
	v_lshl_add_u32 v53, v6, 2, 0
	ds_read_b32 v7, v7 offset:32896
	ds_read_b32 v53, v53 offset:32896
	v_readlane_b32 s4, v254, 54
	v_readlane_b32 s5, v254, 55
	v_add_u32_e32 v54, s29, v9
	s_waitcnt lgkmcnt(1)
	v_add_u32_e32 v56, v7, v4
	s_waitcnt lgkmcnt(0)
	v_add_u32_e32 v58, v53, v5
	v_lshlrev_b64 v[4:5], 17, v[2:3]
	v_ashrrev_i32_e32 v57, 31, v56
	v_lshl_add_u64 v[4:5], s[4:5], 0, v[4:5]
	v_lshl_add_u64 v[4:5], v[56:57], 2, v[4:5]
	v_ashrrev_i32_e32 v7, 31, v6
	global_store_dword v[4:5], v54, off sc1
	v_lshlrev_b64 v[4:5], 17, v[6:7]
	v_ashrrev_i32_e32 v59, 31, v58
	v_lshl_add_u64 v[4:5], s[4:5], 0, v[4:5]
	v_lshl_add_u64 v[4:5], v[58:59], 2, v[4:5]
	v_ashrrev_i32_e32 v55, 31, v54
	v_readlane_b32 s4, v254, 52
	global_store_dword v[4:5], v54, off sc1
	v_lshlrev_b64 v[4:5], 5, v[54:55]
	v_readlane_b32 s5, v254, 53
	v_mov_b32_e32 v7, v58
	s_nop 0
	v_lshl_add_u64 v[54:55], s[4:5], 0, v[4:5]
	v_mov_b32_e32 v4, v2
	v_mov_b32_e32 v5, v56
	v_mov_b32_e32 v2, v3
	global_store_dwordx4 v[54:55], v[4:7], off sc1
	global_store_dwordx4 v[54:55], v[0:3], off offset:16 sc1
	s_branch .LBB0_3232
